# speedup vs baseline: 1.0266x; 1.0053x over previous
_Z16sum_layer_kernelPKfS0_Pf:
	s_load_dwordx4 s[4:7], s[0:1], 0x0
	s_load_dwordx2 s[8:9], s[0:1], 0x10
	v_lshrrev_b32_e32 v42, 6, v0
	v_bfe_u32 v41, v0, 5, 1
	v_and_b32_e32 v40, 31, v0
	v_readfirstlane_b32 s23, v42
	v_and_b32_e32 v43, 7, v0
	v_bfe_u32 v44, v0, 3, 3
	s_lshl_b32 s3, s2, 12
	s_lshl_b32 s19, s2, 7
	s_lshl_b32 s23, s23, 12
	v_lshlrev_b32_e32 v1, 11, v41
	v_lshl_or_b32 v1, v40, 2, v1
	s_mov_b32 m0, s23
	v_lshrrev_b32_e32 v46, 1, v44
	v_xor_b32_e32 v46, v43, v46
	v_lshlrev_b32_e32 v46, 4, v46
	v_lshl_add_u32 v35, v44, 16, v46
	v_lshl_add_u32 v35, v42, 21, v35
	v_add_u32_e32 v35, s19, v35
	v_xor_b32_e32 v86, 64, v35
	s_mov_b32 s20, 0x7fc00
	s_mov_b32 s21, 0xff800
	s_mov_b32 s22, 0x17f400
	s_mov_b32 s14, 0x200000
	s_mov_b32 s15, 0x20000
	v_and_b32_e32 v45, 63, v0
	v_lshlrev_b32_e32 v37, 4, v45
	s_add_u32 s54, s23, 0x4000
	s_waitcnt lgkmcnt(0)
	s_mov_b32 s12, s6
	s_and_b32 s13, s7, 0xffff
	s_and_b32 s5, s5, 0xffff
	s_mov_b32 s6, 0x800000
	s_mov_b32 s7, s15
	s_mov_b32 m0, s54
	s_nop 0
	buffer_load_dwordx4 v37, s[12:15], s3 offen nt lds
	buffer_load_dwordx4 v37, s[12:15], s3 offen offset:1024 nt lds
	buffer_load_dwordx4 v37, s[12:15], s3 offen offset:2048 nt lds
	buffer_load_dwordx4 v37, s[12:15], s3 offen offset:3072 nt lds
	s_mov_b32 m0, s23
	s_nop 0
	buffer_load_dwordx4 v35, s[4:7], 0 offen nt lds
	buffer_load_dwordx4 v86, s[4:7], s20 offen offset:1024 nt lds
	buffer_load_dwordx4 v35, s[4:7], s21 offen offset:2048 nt lds
	buffer_load_dwordx4 v86, s[4:7], s22 offen offset:3072 nt lds
	v_and_b32_e32 v45, 63, v0
	v_and_b32_e32 v36, 30, v40
	v_lshlrev_b32_e32 v36, 2, v36
	v_and_b32_e32 v47, 1, v40
	v_lshl_add_u32 v36, v47, 16, v36
	v_lshl_add_u32 v36, v41, 18, v36
	v_lshl_add_u32 v36, v42, 21, v36
	v_add_u32_e32 v36, s19, v36
	v_bfe_u32 v47, v40, 1, 3
	v_lshlrev_b32_e32 v39, 2, v41
	v_xor_b32_e32 v39, v39, v47
	v_lshlrev_b32_e32 v39, 4, v39
	v_lshl_add_u32 v39, v40, 7, v39
	v_lshl_add_u32 v39, v42, 12, v39
	v_xor_b32_e32 v81, 16, v39
	v_xor_b32_e32 v82, 32, v39
	v_xor_b32_e32 v83, 48, v39
	v_cmp_gt_u32_e32 vcc, 32, v45
	v_mov_b32_e32 v34, 0xc1600000
	v_mov_b32_e32 v84, 0x3fb8aa3b
	v_mov_b32_e32 v85, 0x3f317218
	s_lshl_b32 s25, 2, 16
	s_lshl_b32 s27, 8, 16
	s_lshl_b32 s29, 10, 16
	s_lshl_b32 s31, 16, 16
	s_lshl_b32 s33, 18, 16
	s_lshl_b32 s35, 24, 16
	s_lshl_b32 s37, 26, 16
	s_mov_b32 s40, 0xaaaaaaaa
	s_mov_b32 s41, 0xaaaaaaaa
	s_mov_b32 s42, 0x55555555
	s_mov_b32 s43, 0x55555555
	s_and_b32 s9, s9, 0xffff
	s_mov_b32 s10, s6
	s_mov_b32 s11, s15
	v_lshl_add_u32 v38, v42, 12, v1
	v_add_u32_e32 v38, 0x4000, v38
	v_add_u32_e32 v87, 0x400, v38
	s_waitcnt vmcnt(4)
	ds_read2_b32 v[18:19], v38 offset0:0 offset1:32
	ds_read2_b32 v[20:21], v38 offset0:64 offset1:96
	ds_read2_b32 v[22:23], v38 offset0:128 offset1:160
	ds_read2_b32 v[24:25], v38 offset0:192 offset1:224
	ds_read2_b32 v[26:27], v87 offset0:0 offset1:32
	ds_read2_b32 v[28:29], v87 offset0:64 offset1:96
	ds_read2_b32 v[30:31], v87 offset0:128 offset1:160
	ds_read2_b32 v[32:33], v87 offset0:192 offset1:224
	s_waitcnt lgkmcnt(0)
	v_max3_f32 v48, v18, v19, v20
	v_max3_f32 v50, v21, v22, v23
	v_max3_f32 v48, v48, v24, v25
	v_max3_f32 v50, v50, v26, v27
	v_max3_f32 v48, v48, v28, v29
	v_max3_f32 v50, v50, v30, v31
	v_max3_f32 v48, v48, v32, v33
	v_max_f32_e32 v48, v48, v50
	v_mov_b32_e32 v50, v48
	s_nop 1
	v_permlane32_swap_b32_e32 v48, v50
	v_max_f32_e32 v48, v48, v50
	v_fmamk_f32 v48, v48, 0x3fb8aa3b, v34
	v_pk_fma_f32 v[18:19], v[18:19], v[84:85], v[48:49] op_sel_hi:[1,0,0] neg_lo:[0,0,1] neg_hi:[0,0,1]
	v_exp_f32_e32 v18, v18
	v_exp_f32_e32 v19, v19
	v_pk_fma_f32 v[20:21], v[20:21], v[84:85], v[48:49] op_sel_hi:[1,0,0] neg_lo:[0,0,1] neg_hi:[0,0,1]
	v_exp_f32_e32 v20, v20
	v_exp_f32_e32 v21, v21
	v_pk_fma_f32 v[22:23], v[22:23], v[84:85], v[48:49] op_sel_hi:[1,0,0] neg_lo:[0,0,1] neg_hi:[0,0,1]
	v_exp_f32_e32 v22, v22
	v_exp_f32_e32 v23, v23
	v_pk_fma_f32 v[24:25], v[24:25], v[84:85], v[48:49] op_sel_hi:[1,0,0] neg_lo:[0,0,1] neg_hi:[0,0,1]
	v_exp_f32_e32 v24, v24
	v_exp_f32_e32 v25, v25
	v_pk_fma_f32 v[26:27], v[26:27], v[84:85], v[48:49] op_sel_hi:[1,0,0] neg_lo:[0,0,1] neg_hi:[0,0,1]
	v_exp_f32_e32 v26, v26
	v_exp_f32_e32 v27, v27
	v_pk_fma_f32 v[28:29], v[28:29], v[84:85], v[48:49] op_sel_hi:[1,0,0] neg_lo:[0,0,1] neg_hi:[0,0,1]
	v_exp_f32_e32 v28, v28
	v_exp_f32_e32 v29, v29
	v_pk_fma_f32 v[30:31], v[30:31], v[84:85], v[48:49] op_sel_hi:[1,0,0] neg_lo:[0,0,1] neg_hi:[0,0,1]
	v_exp_f32_e32 v30, v30
	v_exp_f32_e32 v31, v31
	v_pk_fma_f32 v[32:33], v[32:33], v[84:85], v[48:49] op_sel_hi:[1,0,0] neg_lo:[0,0,1] neg_hi:[0,0,1]
	v_exp_f32_e32 v32, v32
	v_exp_f32_e32 v33, v33
	v_pk_add_f32 v[56:57], v[18:19], v[20:21]
	v_pk_add_f32 v[58:59], v[22:23], v[24:25]
	v_pk_add_f32 v[60:61], v[26:27], v[28:29]
	v_pk_add_f32 v[62:63], v[30:31], v[32:33]
	v_pk_add_f32 v[56:57], v[56:57], v[58:59]
	v_pk_add_f32 v[60:61], v[60:61], v[62:63]
	v_pk_add_f32 v[56:57], v[56:57], v[60:61]
	v_add_f32_e32 v50, v56, v57
	v_mov_b32_e32 v51, v50
	s_nop 1
	v_permlane32_swap_b32_e32 v50, v51
	v_add_f32_e32 v50, v50, v51
	v_log_f32_e32 v50, v50
	v_cvt_pk_f16_f32 v40, v18, v19
	v_cvt_pk_f16_f32 v41, v20, v21
	v_cvt_pk_f16_f32 v42, v22, v23
	v_cvt_pk_f16_f32 v43, v24, v25
	v_cvt_pk_f16_f32 v44, v26, v27
	v_cvt_pk_f16_f32 v45, v28, v29
	v_cvt_pk_f16_f32 v46, v30, v31
	v_cvt_pk_f16_f32 v47, v32, v33
	v_add_f32_e32 v50, 0x41600000, v50
	v_mul_f32_e32 v50, 0xbf317218, v50
	v_cndmask_b32_e64 v51, v50, 1.0, vcc
	s_waitcnt vmcnt(0)
	ds_read_b128 v[2:5], v39
	ds_read_b128 v[6:9], v81
	ds_read_b128 v[10:13], v82
	ds_read_b128 v[14:17], v83
	s_waitcnt lgkmcnt(2)
	v_max3_f32 v52, v2, v3, v4
	v_max3_f32 v53, v5, v6, v7
	v_max_f32_e32 v52, v52, v8
	v_max_f32_e32 v53, v53, v9
	s_waitcnt lgkmcnt(0)
	v_max3_f32 v52, v52, v10, v11
	v_max3_f32 v53, v53, v12, v13
	v_max3_f32 v52, v52, v14, v15
	v_max3_f32 v53, v53, v16, v17
	v_max_f32_e32 v52, v52, v53
	v_mov_b32_e32 v53, v52
	s_nop 1
	v_permlane32_swap_b32_e32 v52, v53
	v_max_f32_e32 v52, v52, v53
	v_cndmask_b32_e32 v54, 1.0, v52, vcc
	v_fmamk_f32 v48, v52, 0x3fb8aa3b, v34
	v_pk_fma_f32 v[2:3], v[2:3], v[84:85], v[48:49] op_sel_hi:[1,0,0] neg_lo:[0,0,1] neg_hi:[0,0,1]
	v_mfma_f32_32x32x2_f32 v[64:79], v54, v51, 0
	v_exp_f32_e32 v2, v2
	v_exp_f32_e32 v3, v3
	v_pk_fma_f32 v[4:5], v[4:5], v[84:85], v[48:49] op_sel_hi:[1,0,0] neg_lo:[0,0,1] neg_hi:[0,0,1]
	v_exp_f32_e32 v4, v4
	v_exp_f32_e32 v5, v5
	v_pk_fma_f32 v[6:7], v[6:7], v[84:85], v[48:49] op_sel_hi:[1,0,0] neg_lo:[0,0,1] neg_hi:[0,0,1]
	v_exp_f32_e32 v6, v6
	v_exp_f32_e32 v7, v7
	v_pk_fma_f32 v[8:9], v[8:9], v[84:85], v[48:49] op_sel_hi:[1,0,0] neg_lo:[0,0,1] neg_hi:[0,0,1]
	v_exp_f32_e32 v8, v8
	v_exp_f32_e32 v9, v9
	v_pk_fma_f32 v[10:11], v[10:11], v[84:85], v[48:49] op_sel_hi:[1,0,0] neg_lo:[0,0,1] neg_hi:[0,0,1]
	v_exp_f32_e32 v10, v10
	v_cvt_pk_f16_f32 v56, v2, v3
	v_cvt_pk_f16_f32 v57, v4, v5
	v_cvt_pk_f16_f32 v58, v6, v7
	v_cvt_pk_f16_f32 v59, v8, v9
	v_exp_f32_e32 v11, v11
	v_pk_fma_f32 v[12:13], v[12:13], v[84:85], v[48:49] op_sel_hi:[1,0,0] neg_lo:[0,0,1] neg_hi:[0,0,1]
	v_exp_f32_e32 v12, v12
	v_mfma_f32_32x32x16_f16 v[18:33], v[56:59], v[40:43], 0
	v_exp_f32_e32 v13, v13
	v_pk_fma_f32 v[14:15], v[14:15], v[84:85], v[48:49] op_sel_hi:[1,0,0] neg_lo:[0,0,1] neg_hi:[0,0,1]
	v_exp_f32_e32 v14, v14
	v_exp_f32_e32 v15, v15
	v_pk_fma_f32 v[16:17], v[16:17], v[84:85], v[48:49] op_sel_hi:[1,0,0] neg_lo:[0,0,1] neg_hi:[0,0,1]
	v_exp_f32_e32 v16, v16
	v_exp_f32_e32 v17, v17
	v_cvt_pk_f16_f32 v60, v10, v11
	v_cvt_pk_f16_f32 v61, v12, v13
	v_cvt_pk_f16_f32 v62, v14, v15
	v_cvt_pk_f16_f32 v63, v16, v17
	s_nop 1
	v_mfma_f32_32x32x16_f16 v[18:33], v[60:63], v[44:47], v[18:33]
	s_nop 11
	v_log_f32_e32 v18, v18
	v_log_f32_e32 v19, v19
	v_log_f32_e32 v20, v20
	v_log_f32_e32 v21, v21
	v_pk_fma_f32 v[64:65], v[18:19], v[84:85], v[64:65] op_sel:[0,1,0] op_sel_hi:[1,1,1]
	v_log_f32_e32 v22, v22
	v_log_f32_e32 v23, v23
	v_pk_fma_f32 v[66:67], v[20:21], v[84:85], v[66:67] op_sel:[0,1,0] op_sel_hi:[1,1,1]
	v_log_f32_e32 v24, v24
	v_log_f32_e32 v25, v25
	s_mov_b64 vcc, s[40:41]
	v_cndmask_b32_dpp v19, v64, v65, vcc quad_perm:[1,0,3,2] row_mask:0xf bank_mask:0xf
	s_mov_b64 vcc, s[42:43]
	v_cndmask_b32_dpp v18, v65, v64, vcc quad_perm:[1,0,3,2] row_mask:0xf bank_mask:0xf
	buffer_store_dwordx2 v[18:19], v36, s[8:11], 0 offen
	v_pk_fma_f32 v[68:69], v[22:23], v[84:85], v[68:69] op_sel:[0,1,0] op_sel_hi:[1,1,1]
	v_log_f32_e32 v26, v26
	v_log_f32_e32 v27, v27
	s_mov_b64 vcc, s[40:41]
	v_cndmask_b32_dpp v21, v66, v67, vcc quad_perm:[1,0,3,2] row_mask:0xf bank_mask:0xf
	s_mov_b64 vcc, s[42:43]
	v_cndmask_b32_dpp v20, v67, v66, vcc quad_perm:[1,0,3,2] row_mask:0xf bank_mask:0xf
	buffer_store_dwordx2 v[20:21], v36, s[8:11], s25 offen
	v_pk_fma_f32 v[70:71], v[24:25], v[84:85], v[70:71] op_sel:[0,1,0] op_sel_hi:[1,1,1]
	v_log_f32_e32 v28, v28
	v_log_f32_e32 v29, v29
	s_mov_b64 vcc, s[40:41]
	v_cndmask_b32_dpp v23, v68, v69, vcc quad_perm:[1,0,3,2] row_mask:0xf bank_mask:0xf
	s_mov_b64 vcc, s[42:43]
	v_cndmask_b32_dpp v22, v69, v68, vcc quad_perm:[1,0,3,2] row_mask:0xf bank_mask:0xf
	buffer_store_dwordx2 v[22:23], v36, s[8:11], s27 offen
	v_pk_fma_f32 v[72:73], v[26:27], v[84:85], v[72:73] op_sel:[0,1,0] op_sel_hi:[1,1,1]
	v_log_f32_e32 v30, v30
	v_log_f32_e32 v31, v31
	s_mov_b64 vcc, s[40:41]
	v_cndmask_b32_dpp v25, v70, v71, vcc quad_perm:[1,0,3,2] row_mask:0xf bank_mask:0xf
	s_mov_b64 vcc, s[42:43]
	v_cndmask_b32_dpp v24, v71, v70, vcc quad_perm:[1,0,3,2] row_mask:0xf bank_mask:0xf
	buffer_store_dwordx2 v[24:25], v36, s[8:11], s29 offen
	v_pk_fma_f32 v[74:75], v[28:29], v[84:85], v[74:75] op_sel:[0,1,0] op_sel_hi:[1,1,1]
	v_log_f32_e32 v32, v32
	v_log_f32_e32 v33, v33
	s_mov_b64 vcc, s[40:41]
	v_cndmask_b32_dpp v27, v72, v73, vcc quad_perm:[1,0,3,2] row_mask:0xf bank_mask:0xf
	s_mov_b64 vcc, s[42:43]
	v_cndmask_b32_dpp v26, v73, v72, vcc quad_perm:[1,0,3,2] row_mask:0xf bank_mask:0xf
	buffer_store_dwordx2 v[26:27], v36, s[8:11], s31 offen
	v_pk_fma_f32 v[76:77], v[30:31], v[84:85], v[76:77] op_sel:[0,1,0] op_sel_hi:[1,1,1]
	s_mov_b64 vcc, s[40:41]
	v_cndmask_b32_dpp v29, v74, v75, vcc quad_perm:[1,0,3,2] row_mask:0xf bank_mask:0xf
	s_mov_b64 vcc, s[42:43]
	v_cndmask_b32_dpp v28, v75, v74, vcc quad_perm:[1,0,3,2] row_mask:0xf bank_mask:0xf
	buffer_store_dwordx2 v[28:29], v36, s[8:11], s33 offen
	v_pk_fma_f32 v[78:79], v[32:33], v[84:85], v[78:79] op_sel:[0,1,0] op_sel_hi:[1,1,1]
	s_mov_b64 vcc, s[40:41]
	v_cndmask_b32_dpp v31, v76, v77, vcc quad_perm:[1,0,3,2] row_mask:0xf bank_mask:0xf
	s_mov_b64 vcc, s[42:43]
	v_cndmask_b32_dpp v30, v77, v76, vcc quad_perm:[1,0,3,2] row_mask:0xf bank_mask:0xf
	buffer_store_dwordx2 v[30:31], v36, s[8:11], s35 offen
	s_nop 0
	s_mov_b64 vcc, s[40:41]
	v_cndmask_b32_dpp v33, v78, v79, vcc quad_perm:[1,0,3,2] row_mask:0xf bank_mask:0xf
	s_mov_b64 vcc, s[42:43]
	v_cndmask_b32_dpp v32, v79, v78, vcc quad_perm:[1,0,3,2] row_mask:0xf bank_mask:0xf
	buffer_store_dwordx2 v[32:33], v36, s[8:11], s37 offen
	s_endpgm
